# PEER coefficient pass (both layers): workgroups start in four groups 1.5 us apart, as in P0
# baseline (speedup 1.0000x reference)
; __device__ __forceinline__ int opaque_i(int v) { asm volatile("" : "+v"(v)); return v; }
; __device__ __forceinline__ void phase_peer_c(Frame& F, const int* PREP, const float* GATE, unsigned char* ACO8, float* ASC  ) {
;     const int gw = F.vcu * NWAVES + F.wave, NGW = F.G * NWAVES, lane = opaque_i(F.lane);
;     for (int t0 = gw * 4; t0 < TOK; t0 += NGW * 4) {
;         int pv[4][4][2]; float gt[4][2];
; #pragma unroll
;         for (int q = 0; q < 4; ++q) {
; #pragma unroll
;             for (int x = 0; x < 4; ++x) { const int* p = PREP + ((size_t)x * TOK + t0 + q) * 128; pv[q][x][0] = p[lane]; pv[q][x][1] = p[64 + lane]; }
;             gt[q][0] = GATE[(size_t)(t0 + q) * 128 + lane]; gt[q][1] = GATE[(size_t)(t0 + q) * 128 + 64 + lane]; }
; #pragma unroll
;         for (int q = 0; q < 4; ++q) { const int t = t0 + q;
;             const int i0 = (pv[q][0][0] + pv[q][1][0]) + (pv[q][2][0] + pv[q][3][0]), i1 = (pv[q][0][1] + pv[q][1][1]) + (pv[q][2][1] + pv[q][3][1]);
;             const float rsu = 1.f / (I4_SU * I8_SX);
;             const float a0 = gelu_erf((float)i0 * rsu) * gt[q][0], a1 = gelu_erf((float)i1 * rsu) * gt[q][1];
;             float m = fmaxf(fabsf(a0), fabsf(a1));
;             m = fmaxf(m, dpp_row_shr(m, 1)); m = fmaxf(m, dpp_row_shr(m, 2)); m = fmaxf(m, dpp_row_shr(m, 4)); m = fmaxf(m, dpp_row_shr(m, 8));
;             m = fmaxf(m, __builtin_bit_cast(float, __builtin_amdgcn_update_dpp(0, __builtin_bit_cast(int, m), 0x142, 0xa, 0xf, false)));
;             m = fmaxf(m, __builtin_bit_cast(float, __builtin_amdgcn_update_dpp(0, __builtin_bit_cast(int, m), 0x143, 0xc, 0xf, false)));
;             m = __builtin_bit_cast(float, __builtin_amdgcn_readlane(__builtin_bit_cast(int, m), 63));
;             const float inv = m > 0.f ? 127.f / m : 0.f;
;             const int q0 = __float2int_rn(a0 * inv), q1 = __float2int_rn(a1 * inv);
;             ACO8[(size_t)t * 128 + lane] = (unsigned char)(q0 & 0xff); ACO8[(size_t)t * 128 + 64 + lane] = (unsigned char)(q1 & 0xff);
;             const float sa = wave_total((float)(q0 + q1)), scl = m * (1.f / (127.f * I4_SV));
;             if (lane == 0) { ASC[2 * (size_t)t] = scl; ASC[2 * (size_t)t + 1] = 8.f * sa * scl; } }
.LBB0_938:
	v_readlane_b32 s0, v237, 4
	v_readlane_b32 s1, v237, 5
	s_cmp_lt_i32 s0, 9
	s_cselect_b64 s[0:1], -1, 0
	s_and_b64 s[4:5], s[0:1], s[2:3]
	s_andn2_b64 vcc, exec, s[4:5]
	s_cbranch_vccnz .LBB0_950
	v_readlane_b32 s98, v237, 3
	s_nop 3
	s_and_b32 s98, s98, 3
.Ldeph_p8:
	s_cmp_eq_u32 s98, 0
	s_cbranch_scc1 .Ldeph_p8_done
	s_sleep 50
	s_sub_u32 s98, s98, 1
	s_branch .Ldeph_p8
.Ldeph_p8_done:
	s_lshl_b32 s0, s73, 5
	s_lshl_b32 s1, s74, 2
	s_add_i32 s0, s0, s1
	v_mov_b32_e32 v2, v208
	s_cmpk_gt_i32 s0, 0x7fff
	s_cbranch_scc1 .LBB0_950
	s_lshl_b32 s6, s72, 5
	s_ashr_i32 s1, s0, 31
	v_ashrrev_i32_e32 v3, 31, v2
	s_ashr_i32 s7, s6, 31
	s_lshl_b64 s[12:13], s[0:1], 7
	s_lshl_b64 s[14:15], s[0:1], 9
	v_cmp_eq_u32_e64 s[2:3], 0, v2
	s_lshl_b64 s[8:9], s[0:1], 3
	s_lshl_b64 s[10:11], s[6:7], 3
	s_waitcnt lgkmcnt(0)
	v_lshl_add_u64 v[0:1], s[12:13], 0, v[2:3]
	s_lshl_b64 s[12:13], s[6:7], 7
	v_lshl_add_u64 v[2:3], v[2:3], 2, s[14:15]
	s_lshl_b64 s[14:15], s[6:7], 9
	s_mov_b32 s1, 0x3e6d3388
	v_mov_b32_e32 v6, 0xbf3a00e3
	s_mov_b32 s7, 0x42fe0000
	v_mov_b32_e32 v7, 0x42fe0000
	s_mov_b32 s18, 0x1a000000
	v_mov_b32_e32 v8, 0x1a800000
	v_mov_b32_e32 v9, 0x3a74908f
	v_mov_b32_e32 v10, 0x41000000
	s_branch .LBB0_942

; __device__ __forceinline__ int opaque_i(int v) { asm volatile("" : "+v"(v)); return v; }
; __device__ __forceinline__ void phase_peer_c(Frame& F, const int* PREP, const float* GATE, unsigned char* ACO8, float* ASC  ) {
;     const int gw = F.vcu * NWAVES + F.wave, NGW = F.G * NWAVES, lane = opaque_i(F.lane);
;     for (int t0 = gw * 4; t0 < TOK; t0 += NGW * 4) {
.LBB0_1697:
	v_readlane_b32 s0, v237, 4
	v_readlane_b32 s1, v237, 5
	s_cmp_lt_i32 s0, 18
	s_cselect_b64 s[0:1], -1, 0
	s_and_b64 s[4:5], s[0:1], s[2:3]
	s_andn2_b64 vcc, exec, s[4:5]
	s_cbranch_vccnz .LBB0_1709
	v_readlane_b32 s98, v237, 3
	s_nop 3
	s_and_b32 s98, s98, 3
